# MoE down-GEMM hand-off: drop the redundant per-unit L1/L2 invalidate after the counter poll (rows of a row tile are never loaded before its counter completes; grid barriers invalidate)
# speedup vs baseline: 1.0286x; 1.0043x over previous
;     __device__ __forceinline__ size_t abase(const Unit& u) const { return (size_t)((hot & 1) ? 0 : u.pm) * BM * K * 2; }
;     __device__ __forceinline__ void a_ready(const Unit& u, int wv) const { if (wready) wait_counter(wready + 64 * u.pm, wneed, wtmo, wv); }
;     __device__ __forceinline__ const char* bbase(const Unit& u) const { return (const char*)Bt + (size_t)((hot & 2) ? 0 : u.pn) * BM * K * 2; }
;     __device__ __forceinline__ const char* bbase(const Unit& u) const { return (const char*)Bt + ((size_t)u.e * bstride + (size_t)u.pn * BM * K) * 2; }
; #define PG8_BAR __builtin_amdgcn_s_barrier()
;     __device__ __forceinline__ void a_ready(const Unit& u, const int wv) const {
;     ...
;                 __builtin_amdgcn_fence(__ATOMIC_ACQUIRE, "agent");
;                 asm volatile("s_waitcnt vmcnt(0)" ::: "memory");
;     ...
;     { int R, C; stage_rc(tid * 16, R, C); const int Rb = Epi::PERM ? ((R & ~31) + perm32(R & 31)) : R; voffB = (unsigned)(Rb * K + C) * 2u; }
;     const size_t bstep = (size_t)64 * K * 2;
;     ...
;     const size_t kstep = (size_t)(BK * 2);
;     const size_t hstep = (size_t)HALF * K * 2;
;     const unsigned ldsw = (unsigned)wid * 1024u;
;     const int aoff = lds_byte(wr * 64 + fr, fq * 8), boff = lds_byte(wc * 32 + fr, fq * 8);
;     const char* Ab = (const char*)Abase;
;     ...
;     Unit cur, nxt; int ui = 0;
;     if (!S.next(0, cur)) return;
;     f32x4 acc[2][2][4][2];
; #pragma unroll
;     for (int a = 0; a < 2; ++a)
; #pragma unroll
;         for (int b = 0; b < 2; ++b)
; #pragma unroll
;             for (int m = 0; m < 4; ++m)
; #pragma unroll
;                 for (int n = 0; n < 2; ++n) acc[a][b][m][n] = (f32x4){0.f, 0.f, 0.f, 0.f};
;     bf16x8 At[4][2], B0[2][2], B1[2][2];
;     constexpr bool DN = Sched::DENSE;
;     unsigned oA0[2], oA1[2], oN0[2], oN1[2];
;     unsigned voffA[2];
;     if constexpr (DN) {
; #pragma unroll
;         for (int i = 0; i < 2; ++i) { int R, C; stage_rc(tid * 16 + i * 8192, R, C); voffA[i] = (unsigned)(R * K + C) * 2u; }
;     } else PG8_AOFFS(cur, oA0, oA1);
;     const char* cA0 = DN ? Ab + S.abase(cur) : Ab;
;     const size_t ah = DN ? hstep : 0;
;     ...
;     const char* cB = S.bbase(cur);
;     S.a_ready(cur, wv);
;     ...
;     PG8_STAGEB(PG8_SB(0, 0), cB); PG8_STAGEB(PG8_SB(0, 1), cB + hstep); PG8_STAGE(PG8_SA(0, 0), cA0, PG8_O0); PG8_STAGE(PG8_SA(0, 1), cA0 + ah, PG8_O1);
;     if (wr == 1) PG8_BAR;
.LBB0_1646:
.LBB0_1647:
	v_mul_i32_i24_e32 v3, 64, v3
	v_sub_u32_e32 v1, v1, v3
	v_lshlrev_b32_e32 v0, 5, v0
	v_ashrrev_i16_sdwa v1, v227, sext(v1) dst_sel:DWORD dst_unused:UNUSED_PAD src0_sel:DWORD src1_sel:BYTE_0
	v_and_b32_e32 v0, 32, v0
	v_bfe_i32 v1, v1, 0, 16
	v_add_lshl_u32 v0, v0, v1, 1
	v_lshlrev_b32_e32 v1, 6, v8
	v_sub_u32_e32 v1, v7, v1
	s_waitcnt vmcnt(3)
	v_lshl_add_u32 v132, v4, 10, v0
	s_waitcnt vmcnt(2)
	v_lshl_add_u32 v134, v5, 10, v0
	v_lshlrev_b32_e32 v0, 5, v6
	v_ashrrev_i16_sdwa v1, v227, sext(v1) dst_sel:DWORD dst_unused:UNUSED_PAD src0_sel:DWORD src1_sel:BYTE_0
	v_and_b32_e32 v0, 32, v0
	v_bfe_i32 v1, v1, 0, 16
	v_add_lshl_u32 v0, v0, v1, 1
	v_bfe_i32 v3, v2, 27, 1
	s_waitcnt vmcnt(1)
	v_lshl_add_u32 v136, v9, 10, v0
	s_waitcnt vmcnt(0)
	v_lshl_add_u32 v138, v10, 10, v0
	v_lshlrev_b32_e32 v0, 4, v2
	v_lshrrev_b32_e32 v3, 22, v3
	v_add_u32_e32 v3, v0, v3
	v_and_b32_e32 v3, 0xfffffc00, v3
	v_sub_u32_e32 v0, v0, v3
	v_ashrrev_i32_e32 v1, 31, v2
	v_lshrrev_b32_e32 v3, 4, v0
	v_lshrrev_b32_e32 v1, 26, v1
	v_bitop3_b32 v3, v3, v0, 32 bitop3:0x6c
	v_ashrrev_i32_e32 v0, 31, v0
	s_add_u32 s39, s8, 0x20400000
	v_add_u32_e32 v1, v2, v1
	v_lshrrev_b32_e32 v0, 26, v0
	s_addc_u32 s45, s9, 0
	s_ashr_i32 s21, s20, 31
	s_ashr_i32 s1, s0, 31
	v_ashrrev_i32_e32 v1, 6, v1
	v_add_u32_e32 v0, v3, v0
	s_lshl_b64 s[2:3], s[20:21], 20
	s_lshl_b64 s[4:5], s[0:1], 18
	v_lshlrev_b32_e32 v4, 3, v1
	v_ashrrev_i32_e32 v0, 6, v0
	s_add_u32 s1, s39, s4
	v_and_b32_e32 v4, -16, v4
	v_mul_i32_i24_e32 v5, 64, v0
	s_addc_u32 s4, s45, s5
	v_add_u32_e32 v4, v0, v4
	v_sub_u32_e32 v3, v3, v5
	s_add_u32 s24, s1, s2
	v_lshlrev_b32_e32 v1, 5, v1
	v_ashrrev_i16_sdwa v3, v227, sext(v3) dst_sel:DWORD dst_unused:UNUSED_PAD src0_sel:DWORD src1_sel:BYTE_0
	v_lshlrev_b32_e32 v5, 1, v4
	v_lshrrev_b32_e32 v6, 2, v4
	v_and_b32_e32 v0, 3, v0
	s_mov_b32 s2, 0x3fffe0
	s_addc_u32 s25, s4, s3
	s_ashr_i32 s1, s16, 6
	v_and_b32_e32 v1, 32, v1
	v_bfe_i32 v3, v3, 0, 16
	v_and_b32_e32 v5, 24, v5
	v_and_b32_e32 v6, 4, v6
	v_and_or_b32 v0, v4, s2, v0
	v_or3_b32 v0, v0, v6, v5
	v_add_lshl_u32 v1, v1, v3, 1
	s_lshl_b32 s21, s1, 10
	v_lshl_add_u32 v130, v0, 10, v1
	v_mov_b32_e32 v131, v65
	s_add_i32 s48, s21, 0x100
	s_barrier
	v_lshl_add_u64 v[0:1], s[24:25], 0, v[130:131]
	s_add_i32 m0, s48, 0x10000
	v_lshl_add_u64 v[4:5], v[0:1], 0, s[82:83]
	global_load_lds_dwordx4 v130, s[24:25]
	s_add_i32 m0, s48, 0x12000
	s_add_i32 s49, s48, 0x2000
	global_load_lds_dwordx4 v[4:5], off
	v_lshl_add_u64 v[4:5], v[0:1], 0, s[66:67]
	s_add_i32 m0, s48, 0x14000
	s_add_i32 s50, s48, 0x4000
	global_load_lds_dwordx4 v[4:5], off
	v_lshl_add_u64 v[4:5], v[0:1], 0, s[84:85]
	s_add_i32 m0, s48, 0x16000
	s_add_i32 s54, s48, 0x6000
	global_load_lds_dwordx4 v[4:5], off
	s_mov_b32 m0, s48
	s_ashr_i32 s4, s16, 8
	global_load_lds_dwordx4 v132, s[10:11]
	s_mov_b32 m0, s49
	s_cmp_eq_u32 s4, 1
	global_load_lds_dwordx4 v136, s[10:11]
	s_mov_b32 m0, s50
	s_cselect_b64 s[2:3], -1, 0
	global_load_lds_dwordx4 v134, s[10:11]
	s_mov_b32 m0, s54
	s_cmp_lg_u32 s4, 1
	global_load_lds_dwordx4 v138, s[10:11]
	s_cbranch_scc1 .LBB0_1649
	s_barrier

;     __device__ __forceinline__ void a_ready(const Unit& u, const int wv) const {
;     ...
;                 __builtin_amdgcn_fence(__ATOMIC_ACQUIRE, "agent");
;                 asm volatile("s_waitcnt vmcnt(0)" ::: "memory");
;             }
;             asm volatile("" ::: "memory"); __builtin_amdgcn_s_barrier(); asm volatile("" ::: "memory");
.LBB0_1659:
.LBB0_1660:
	s_barrier
